# norm1: next row x loads prefetched one iteration ahead into shadow registers
# baseline (speedup 1.0000x reference)
; __device__ __forceinline__ void ph_norm1_tables(const Params& p) {
;     ...
;     for (int it = blockIdx.x; it < N1_ROWITEMS; it += gridDim.x) {
;         {
;             const int row = it * 8 + wave; const int rr = row < NLAT ? (row >> 11) : 4;
;             const float* xr = row < NLAT ? p.in[I_X] + (size_t)row * DM : p.in[I_CTX] + (size_t)(row - NLAT) * DM;
;             f32x4 x[8], y[8];
; #pragma unroll
;             for (int j = 0; j < 8; ++j) x[j] = *(const f32x4*)(xr + j * 256 + lane * 4);
.LBB0_144:
	s_cmp_lt_i32 s86, 2
	s_cselect_b64 s[2:3], -1, 0
	s_and_b64 s[0:1], s[2:3], s[0:1]
	s_andn2_b64 vcc, exec, s[0:1]
	s_cbranch_vccnz .LBB0_152
	s_cmpk_gt_i32 s92, 0x47f
	v_mov_b32_e32 v1, v0
	s_mov_b64 s[0:1], 0
	s_cbranch_scc1 .LBB0_152
	v_ashrrev_i32_e32 v3, 6, v1
	v_lshlrev_b32_e32 v1, 2, v1
	v_and_b32_e32 v2, 0xfc, v1
	v_mbcnt_lo_u32_b32 v1, -1, 0
	v_mbcnt_hi_u32_b32 v4, -1, v1
	v_and_b32_e32 v1, 64, v4
	v_add_u32_e32 v5, 64, v1
	v_readlane_b32 s8, v251, 0
	v_mov_b32_e32 v39, 0
	v_or_b32_e32 v10, 0x400, v2
	v_lshlrev_b32_e32 v38, 2, v2
	v_readlane_b32 s16, v251, 8
	v_readlane_b32 s17, v251, 9
	v_or_b32_e32 v12, 0x500, v2
	v_lshl_add_u64 v[40:41], s[16:17], 0, v[38:39]
	v_lshlrev_b32_e32 v38, 2, v10
	v_or_b32_e32 v14, 0x600, v2
	v_lshl_add_u64 v[42:43], s[16:17], 0, v[38:39]
	v_lshlrev_b32_e32 v38, 2, v12
	s_add_u32 s4, s84, s0
	v_xor_b32_e32 v6, 1, v4
	v_or_b32_e32 v16, 0x700, v2
	v_lshl_add_u64 v[44:45], s[16:17], 0, v[38:39]
	v_lshlrev_b32_e32 v38, 2, v14
	s_addc_u32 s5, s85, s1
	v_cmp_lt_i32_e32 vcc, v6, v5
	v_lshl_add_u64 v[46:47], s[16:17], 0, v[38:39]
	v_lshlrev_b32_e32 v38, 2, v16
	s_add_u32 s0, s4, 0x10000
	v_lshl_add_u64 v[48:49], s[16:17], 0, v[38:39]
	v_lshlrev_b32_e32 v38, 1, v2
	s_addc_u32 s1, s5, 0
	v_or_b32_e32 v4, 0x100, v2
	v_or_b32_e32 v6, 0x200, v2
	v_or_b32_e32 v8, 0x300, v2
	v_readlane_b32 s9, v251, 1
	v_readlane_b32 s10, v251, 2
	v_readlane_b32 s11, v251, 3
	v_readlane_b32 s12, v251, 4
	v_lshl_add_u64 v[18:19], s[4:5], 0, v[38:39]
	s_mov_b64 s[4:5], 0x1cdb8000
	v_lshl_add_u64 v[50:51], v[18:19], 0, s[4:5]
	v_lshl_add_u32 v52, s92, 3, v3
	s_lshl_b32 s8, s94, 3
	s_movk_i32 s9, 0x1fff
	v_lshlrev_b32_e32 v54, 2, v2
	s_movk_i32 s10, 0x1000
	s_mov_b64 s[4:5], 0x2000
	v_mov_b32_e32 v73, 0x358637bd
	s_mov_b32 s11, 0x800000
	v_lshlrev_b32_e32 v56, 2, v4
	v_lshlrev_b32_e32 v38, 2, v6
	v_lshlrev_b32_e32 v58, 2, v8
	v_lshlrev_b32_e32 v60, 2, v10
	v_lshlrev_b32_e32 v62, 2, v12
	v_lshlrev_b32_e32 v64, 2, v14
	v_lshlrev_b32_e32 v66, 2, v16
	v_mov_b32_e32 v55, v39
	v_mov_b32_e32 v57, v39
	s_mov_b32 s12, s92
	v_readlane_b32 s13, v251, 5
	v_readlane_b32 s14, v251, 6
	v_readlane_b32 s15, v251, 7
	v_readlane_b32 s18, v251, 10
	v_readlane_b32 s19, v251, 11
	v_readlane_b32 s20, v251, 12
	v_readlane_b32 s21, v251, 13
	v_readlane_b32 s22, v251, 14
	v_readlane_b32 s23, v251, 15
	v_readlane_b32 s98, v251, 0
	v_readlane_b32 s99, v251, 1
	s_nop 1
	v_mov_b32_e32 v218, s98
	v_mov_b32_e32 v219, s99
	v_readlane_b32 s98, v251, 4
	v_readlane_b32 s99, v251, 5
	s_nop 1
	v_mov_b32_e32 v220, s98
	v_mov_b32_e32 v221, s99
	s_mov_b32 s96, -1
	v_and_b32_e32 v208, s96, v52
	v_cmp_lt_i32_e32 vcc, s9, v208
	v_add_u32_e32 v210, 0xffffe000, v208
	s_nop 0
	v_cndmask_b32_e32 v210, v208, v210, vcc
	v_cndmask_b32_e32 v212, v218, v220, vcc
	v_cndmask_b32_e32 v213, v219, v221, vcc
	v_mov_b32_e32 v211, 0
	v_lshlrev_b64 v[214:215], 13, v[210:211]
	v_lshl_add_u64 v[214:215], v[214:215], 0, v[212:213]
	v_lshl_add_u64 v[214:215], v[214:215], 0, v[54:55]
	global_load_dwordx4 v[172:175], v[214:215], off
	global_load_dwordx4 v[176:179], v[214:215], off offset:1024
	global_load_dwordx4 v[180:183], v[214:215], off offset:2048
	global_load_dwordx4 v[184:187], v[214:215], off offset:3072
	v_add_co_u32_e32 v216, vcc, s10, v214
	s_nop 1
	v_addc_co_u32_e32 v217, vcc, 0, v215, vcc
	global_load_dwordx4 v[188:191], v[216:217], off
	global_load_dwordx4 v[192:195], v[216:217], off offset:1024
	global_load_dwordx4 v[196:199], v[216:217], off offset:2048
	global_load_dwordx4 v[200:203], v[216:217], off offset:3072
	s_waitcnt vmcnt(0)
	s_branch .Ln1_top2

; __device__ __forceinline__ void rms_mod_store(const f32x4 (&x)[8], const float* g, const float* scale, const float* shift, bf16_t* orow, f32x4 (&y)[8], int lane) {
;     float ss = 0.f;
; #pragma unroll
;     for (int j = 0; j < 8; ++j) ss += x[j][0] * x[j][0] + x[j][1] * x[j][1] + x[j][2] * x[j][2] + x[j][3] * x[j][3];
;     ss = wave_sum(ss);
;     const float rinv = rsqrtf(ss * (1.0f / DM) + EPS);
; __device__ __forceinline__ void ph_norm1_tables(const Params& p) {
;     ...
;         {
;             const int row = it * 8 + wave; const int rr = row < NLAT ? (row >> 11) : 4;
;             const float* xr = row < NLAT ? p.in[I_X] + (size_t)row * DM : p.in[I_CTX] + (size_t)(row - NLAT) * DM;
;             f32x4 x[8], y[8];
; #pragma unroll
;             for (int j = 0; j < 8; ++j) x[j] = *(const f32x4*)(xr + j * 256 + lane * 4);
;             const float* m = mod + (size_t)rr * 12288;
;             rms_mod_store(x, p.in[I_N1G], m + DM, m, (bf16_t*)(ws + WS_H) + (size_t)row * DM, y, lane);
.Ln1_top2:
	s_nop 1
	v_mov_b32_e32 v53, v39
	v_mov_b32_e32 v30, v172
	v_mov_b32_e32 v31, v173
	v_mov_b32_e32 v32, v174
	v_mov_b32_e32 v33, v175
	v_mov_b32_e32 v26, v176
	v_mov_b32_e32 v27, v177
	v_mov_b32_e32 v28, v178
	v_mov_b32_e32 v29, v179
	v_mov_b32_e32 v22, v180
	v_mov_b32_e32 v23, v181
	v_mov_b32_e32 v24, v182
	v_mov_b32_e32 v25, v183
	v_mov_b32_e32 v14, v184
	v_mov_b32_e32 v15, v185
	v_mov_b32_e32 v16, v186
	v_mov_b32_e32 v17, v187
	v_mov_b32_e32 v18, v188
	v_mov_b32_e32 v19, v189
	v_mov_b32_e32 v20, v190
	v_mov_b32_e32 v21, v191
	v_mov_b32_e32 v10, v192
	v_mov_b32_e32 v11, v193
	v_mov_b32_e32 v12, v194
	v_mov_b32_e32 v13, v195
	v_mov_b32_e32 v6, v196
	v_mov_b32_e32 v7, v197
	v_mov_b32_e32 v8, v198
	v_mov_b32_e32 v9, v199
	v_mov_b32_e32 v2, v200
	v_mov_b32_e32 v3, v201
	v_mov_b32_e32 v4, v202
	v_mov_b32_e32 v5, v203
	v_min_i32_e32 v65, 0x2000, v52
	s_nop 0
	s_nop 0
	v_ashrrev_i32_e32 v65, 11, v65
	v_mul_hi_i32_i24_e32 v95, 0xc000, v65
	v_mul_i32_i24_e32 v94, 0xc000, v65
	v_lshl_add_u64 v[162:163], s[0:1], 0, v[94:95]
	v_mov_b32_e32 v59, v39
	v_lshl_add_u64 v[158:159], v[162:163], 0, s[4:5]
	v_lshl_add_u64 v[114:115], v[158:159], 0, v[58:59]
	v_mov_b32_e32 v61, v39
	v_lshl_add_u64 v[122:123], v[162:163], 0, v[54:55]
	v_lshl_add_u64 v[102:103], v[158:159], 0, v[54:55]
	v_lshl_add_u64 v[118:119], v[158:159], 0, v[56:57]
	v_lshl_add_u64 v[110:111], v[158:159], 0, v[38:39]
	v_lshl_add_u64 v[126:127], v[158:159], 0, v[60:61]
	global_load_dwordx4 v[34:37], v[40:41], off
	global_load_dwordx4 v[74:77], v[40:41], off offset:1024
	global_load_dwordx4 v[78:81], v[40:41], off offset:2048
	global_load_dwordx4 v[82:85], v[40:41], off offset:3072
	global_load_dwordx4 v[86:89], v[42:43], off
	global_load_dwordx4 v[90:93], v[44:45], off
	v_mov_b32_e32 v63, v39
	global_load_dwordx4 v[94:97], v[122:123], off offset:1024
	global_load_dwordx4 v[98:101], v[122:123], off offset:2048
	s_nop 0
	global_load_dwordx4 v[102:105], v[102:103], off
	s_nop 0
	global_load_dwordx4 v[106:109], v[122:123], off
	s_nop 0
	global_load_dwordx4 v[110:113], v[110:111], off
	s_nop 0
	global_load_dwordx4 v[114:117], v[114:115], off
	s_nop 0
	global_load_dwordx4 v[118:121], v[118:119], off
	s_nop 0
	global_load_dwordx4 v[122:125], v[122:123], off offset:3072
	s_nop 0
	global_load_dwordx4 v[126:129], v[126:127], off
	v_lshlrev_b64 v[166:167], 12, v[52:53]
	s_add_i32 s12, s12, s94
	s_cmpk_lt_i32 s12, 0x480
	v_add_u32_e32 v52, s8, v52
	s_waitcnt vmcnt(22)
	v_mul_f32_e32 v59, v31, v31
	s_waitcnt vmcnt(21)
	v_mul_f32_e32 v65, v27, v27
	s_waitcnt vmcnt(20)
	v_mul_f32_e32 v67, v23, v23
	v_fmac_f32_e32 v59, v30, v30
	v_fmac_f32_e32 v65, v26, v26
	s_waitcnt vmcnt(19)
	v_mul_f32_e32 v146, v15, v15
	v_fmac_f32_e32 v67, v22, v22
	v_fmac_f32_e32 v59, v32, v32
	v_fmac_f32_e32 v65, v28, v28
	s_waitcnt vmcnt(18)
	v_mov_b32_e32 v132, v11
	s_waitcnt vmcnt(17)
	v_mov_b32_e32 v133, v19
	v_fmac_f32_e32 v146, v14, v14
	v_fmac_f32_e32 v67, v24, v24
	v_mov_b32_e32 v130, v10
	v_mov_b32_e32 v131, v18
	v_fmac_f32_e32 v59, v33, v33
	v_fmac_f32_e32 v65, v29, v29
	v_pk_mul_f32 v[132:133], v[132:133], v[132:133]
	v_fmac_f32_e32 v146, v16, v16
	v_mov_b32_e32 v134, v12
	v_mov_b32_e32 v135, v20
	s_waitcnt vmcnt(16)
	v_mov_b32_e32 v140, v3
	s_waitcnt vmcnt(15)
	v_mov_b32_e32 v141, v7
	v_fmac_f32_e32 v67, v25, v25
	v_add_f32_e32 v59, v59, v65
	v_pk_fma_f32 v[130:131], v[130:131], v[130:131], v[132:133]
	v_mov_b32_e32 v136, v13
	v_mov_b32_e32 v137, v21
	v_mov_b32_e32 v138, v2
	v_mov_b32_e32 v139, v6
	v_fmac_f32_e32 v146, v17, v17
	v_pk_mul_f32 v[140:141], v[140:141], v[140:141]
	v_add_f32_e32 v59, v67, v59
	v_pk_fma_f32 v[130:131], v[134:135], v[134:135], v[130:131]
	v_mov_b32_e32 v142, v4
	v_mov_b32_e32 v143, v8
	v_pk_fma_f32 v[132:133], v[138:139], v[138:139], v[140:141]
	v_add_f32_e32 v59, v146, v59
	v_pk_fma_f32 v[130:131], v[136:137], v[136:137], v[130:131]
	v_mov_b32_e32 v144, v5
	v_mov_b32_e32 v145, v9
	v_pk_fma_f32 v[132:133], v[142:143], v[142:143], v[132:133]
	v_add_f32_e32 v59, v131, v59
	v_pk_fma_f32 v[132:133], v[144:145], v[144:145], v[132:133]
	v_add_f32_e32 v59, v130, v59
	v_add_f32_e32 v59, v133, v59
	v_add_f32_e32 v59, v132, v59
	v_mov_b32_e32 v67, v59
	s_nop 1
	v_permlane32_swap_b32_e32 v67, v59
	v_lshl_add_u64 v[130:131], v[162:163], 0, v[60:61]
	v_lshl_add_u64 v[138:139], v[158:159], 0, v[62:63]
	global_load_dwordx4 v[130:133], v[130:131], off
	s_nop 0
	global_load_dwordx4 v[134:137], v[46:47], off
	v_mov_b32_e32 v65, v39
	s_waitcnt lgkmcnt(0)
	v_add_f32_e32 v59, v59, v67
	global_load_dwordx4 v[138:141], v[138:139], off
	v_lshl_add_u64 v[142:143], v[162:163], 0, v[62:63]
	v_mov_b32_e32 v67, v39
	global_load_dwordx4 v[142:145], v[142:143], off
	v_lshl_add_u64 v[150:151], v[162:163], 0, v[64:65]
	v_lshl_add_u64 v[146:147], v[158:159], 0, v[64:65]
	v_lshl_add_u64 v[158:159], v[158:159], 0, v[66:67]
	global_load_dwordx4 v[146:149], v[146:147], off
	s_nop 0
	global_load_dwordx4 v[150:153], v[150:151], off
	v_lshl_add_u64 v[162:163], v[162:163], 0, v[66:67]
	global_load_dwordx4 v[154:157], v[48:49], off
	v_mov_b32_e32 v61, v59
	s_nop 1
	v_permlane16_swap_b32_e32 v61, v59
	global_load_dwordx4 v[158:161], v[158:159], off
	s_waitcnt vmcnt(14)
; __device__ __forceinline__ unsigned cvt_pk_bf16(float lo, float hi) { const f32x2 v = {lo, hi}; const bf16x2_t b = __builtin_convertvector(v, bf16x2_t); return __builtin_bit_cast(unsigned, b); }
; __device__ __forceinline__ void rms_mod_store(const f32x4 (&x)[8], const float* g, const float* scale, const float* shift, bf16_t* orow, f32x4 (&y)[8], int lane) {
;     ...
; #pragma unroll
;     for (int j = 0; j < 8; ++j) { const int c = j * 256 + lane * 4;
;         const f32x4 gv = *(const f32x4*)(g + c), sc = *(const f32x4*)(scale + c), sh = *(const f32x4*)(shift + c);
;         y[j] = x[j] * rinv * gv * (1.0f + sc) + sh; }
; #pragma unroll
;     for (int j = 0; j < 8; ++j) { const int c = j * 256 + lane * 4; u32x2 w; w.x = cvt_pk_bf16(y[j][0], y[j][1]); w.y = cvt_pk_bf16(y[j][2], y[j][3]); *(u32x2*)(orow + c) = w; }
; __device__ __forceinline__ void ph_norm1_tables(const Params& p) {
;     ...
;     for (int it = blockIdx.x; it < N1_ROWITEMS; it += gridDim.x) {
;         {
;             const int row = it * 8 + wave; const int rr = row < NLAT ? (row >> 11) : 4;
;             const float* xr = row < NLAT ? p.in[I_X] + (size_t)row * DM : p.in[I_CTX] + (size_t)(row - NLAT) * DM;
;             f32x4 x[8], y[8];
; #pragma unroll
;             for (int j = 0; j < 8; ++j) x[j] = *(const f32x4*)(xr + j * 256 + lane * 4);
;             const float* m = mod + (size_t)rr * 12288;
;             rms_mod_store(x, p.in[I_N1G], m + DM, m, (bf16_t*)(ws + WS_H) + (size_t)row * DM, y, lane);
	v_pk_add_f32 v[104:105], v[104:105], 1.0 op_sel_hi:[1,0]
	global_load_dwordx4 v[162:165], v[162:163], off
	s_cselect_b32 s96, -1, 0
	v_and_b32_e32 v208, s96, v52
	v_cmp_lt_i32_e32 vcc, s9, v208
	v_add_u32_e32 v210, 0xffffe000, v208
	s_nop 0
	v_cndmask_b32_e32 v210, v208, v210, vcc
	v_cndmask_b32_e32 v212, v218, v220, vcc
	v_cndmask_b32_e32 v213, v219, v221, vcc
	v_mov_b32_e32 v211, 0
	v_lshlrev_b64 v[214:215], 13, v[210:211]
	v_lshl_add_u64 v[214:215], v[214:215], 0, v[212:213]
	v_lshl_add_u64 v[214:215], v[214:215], 0, v[54:55]
	global_load_dwordx4 v[172:175], v[214:215], off
	global_load_dwordx4 v[176:179], v[214:215], off offset:1024
	global_load_dwordx4 v[180:183], v[214:215], off offset:2048
	global_load_dwordx4 v[184:187], v[214:215], off offset:3072
	v_add_co_u32_e32 v216, vcc, s10, v214
	s_nop 1
	v_addc_co_u32_e32 v217, vcc, 0, v215, vcc
	global_load_dwordx4 v[188:191], v[216:217], off
	global_load_dwordx4 v[192:195], v[216:217], off offset:1024
	global_load_dwordx4 v[196:199], v[216:217], off offset:2048
	global_load_dwordx4 v[200:203], v[216:217], off offset:3072
	v_pk_add_f32 v[102:103], v[102:103], 1.0 op_sel_hi:[1,0]
	s_waitcnt lgkmcnt(0)
	v_add_f32_e32 v59, v59, v61
	s_nop 1
	v_mov_b32_dpp v61, v59 row_ror:8 row_mask:0xf bank_mask:0xf
	s_waitcnt lgkmcnt(0)
	v_add_f32_e32 v59, v59, v61
	s_nop 1
	v_mov_b32_dpp v61, v59 row_shl:4 row_mask:0xf bank_mask:0x5
	v_mov_b32_dpp v61, v59 row_shr:4 row_mask:0xf bank_mask:0xa
	s_waitcnt lgkmcnt(0)
	v_add_f32_e32 v59, v59, v61
	s_nop 1
	v_mov_b32_dpp v61, v59 quad_perm:[2,3,0,1] row_mask:0xf bank_mask:0xf
	s_waitcnt lgkmcnt(0)
	v_add_f32_e32 v59, v59, v61
	s_nop 1
	v_mov_b32_dpp v61, v59 quad_perm:[1,0,3,2] row_mask:0xf bank_mask:0xf
	s_waitcnt lgkmcnt(0)
	v_add_f32_e32 v59, v59, v61
	v_fmamk_f32 v59, v59, 0x3a000000, v73
	v_mul_f32_e32 v61, 0x4b800000, v59
	v_cmp_gt_f32_e32 vcc, s11, v59
	s_nop 1
	v_cndmask_b32_e32 v59, v59, v61, vcc
	v_rsq_f32_e32 v59, v59
	s_nop 0
	v_mul_f32_e32 v53, 0x45800000, v59
	v_cndmask_b32_e32 v168, v59, v53, vcc
	v_pk_mul_f32 v[32:33], v[32:33], v[168:169] op_sel_hi:[1,0]
	v_pk_mul_f32 v[30:31], v[30:31], v[168:169] op_sel_hi:[1,0]
	v_pk_mul_f32 v[28:29], v[28:29], v[168:169] op_sel_hi:[1,0]
	v_pk_mul_f32 v[26:27], v[26:27], v[168:169] op_sel_hi:[1,0]
	v_pk_mul_f32 v[30:31], v[34:35], v[30:31]
	v_pk_mul_f32 v[32:33], v[36:37], v[32:33]
	v_pk_mul_f32 v[26:27], v[74:75], v[26:27]
	v_pk_mul_f32 v[28:29], v[76:77], v[28:29]
	s_waitcnt vmcnt(19)
	v_pk_add_f32 v[34:35], v[120:121], 1.0 op_sel_hi:[1,0]
	v_pk_add_f32 v[36:37], v[118:119], 1.0 op_sel_hi:[1,0]
	v_pk_mul_f32 v[24:25], v[24:25], v[168:169] op_sel_hi:[1,0]
	v_pk_mul_f32 v[22:23], v[22:23], v[168:169] op_sel_hi:[1,0]
	v_pk_fma_f32 v[28:29], v[34:35], v[28:29], v[96:97]
	v_pk_fma_f32 v[26:27], v[36:37], v[26:27], v[94:95]
	v_pk_mul_f32 v[22:23], v[78:79], v[22:23]
	v_pk_mul_f32 v[24:25], v[80:81], v[24:25]
	v_pk_add_f32 v[34:35], v[112:113], 1.0 op_sel_hi:[1,0]
	v_pk_add_f32 v[36:37], v[110:111], 1.0 op_sel_hi:[1,0]
	v_pk_mul_f32 v[16:17], v[16:17], v[168:169] op_sel_hi:[1,0]
	v_pk_mul_f32 v[14:15], v[14:15], v[168:169] op_sel_hi:[1,0]
	v_pk_fma_f32 v[24:25], v[34:35], v[24:25], v[100:101]
	v_pk_fma_f32 v[22:23], v[36:37], v[22:23], v[98:99]
	v_pk_mul_f32 v[14:15], v[82:83], v[14:15]
	v_pk_mul_f32 v[16:17], v[84:85], v[16:17]
	v_pk_add_f32 v[34:35], v[116:117], 1.0 op_sel_hi:[1,0]
	v_pk_add_f32 v[36:37], v[114:115], 1.0 op_sel_hi:[1,0]
	v_pk_mul_f32 v[20:21], v[20:21], v[168:169] op_sel_hi:[1,0]
	v_pk_mul_f32 v[18:19], v[18:19], v[168:169] op_sel_hi:[1,0]
	s_waitcnt vmcnt(18)
	v_pk_fma_f32 v[16:17], v[34:35], v[16:17], v[124:125]
	v_pk_fma_f32 v[14:15], v[36:37], v[14:15], v[122:123]
	v_pk_mul_f32 v[18:19], v[86:87], v[18:19]
	v_pk_mul_f32 v[20:21], v[88:89], v[20:21]
	s_waitcnt vmcnt(17)
	v_pk_add_f32 v[34:35], v[128:129], 1.0 op_sel_hi:[1,0]
	v_pk_add_f32 v[36:37], v[126:127], 1.0 op_sel_hi:[1,0]
	v_pk_mul_f32 v[12:13], v[12:13], v[168:169] op_sel_hi:[1,0]
	v_pk_mul_f32 v[10:11], v[10:11], v[168:169] op_sel_hi:[1,0]
	s_waitcnt vmcnt(16)
	v_pk_fma_f32 v[20:21], v[34:35], v[20:21], v[132:133]
	v_pk_fma_f32 v[18:19], v[36:37], v[18:19], v[130:131]
	v_pk_mul_f32 v[10:11], v[10:11], v[90:91]
	v_pk_mul_f32 v[12:13], v[12:13], v[92:93]
	s_waitcnt vmcnt(14)
	v_pk_add_f32 v[34:35], v[140:141], 1.0 op_sel_hi:[1,0]
	v_pk_add_f32 v[36:37], v[138:139], 1.0 op_sel_hi:[1,0]
	v_pk_mul_f32 v[8:9], v[8:9], v[168:169] op_sel_hi:[1,0]
	v_pk_mul_f32 v[6:7], v[6:7], v[168:169] op_sel_hi:[1,0]
	s_waitcnt vmcnt(13)
	v_pk_fma_f32 v[12:13], v[12:13], v[34:35], v[144:145]
	v_pk_fma_f32 v[10:11], v[10:11], v[36:37], v[142:143]
	v_pk_mul_f32 v[6:7], v[6:7], v[134:135]
	v_pk_mul_f32 v[8:9], v[8:9], v[136:137]
	s_waitcnt vmcnt(12)
	v_pk_add_f32 v[34:35], v[148:149], 1.0 op_sel_hi:[1,0]
	v_pk_add_f32 v[36:37], v[146:147], 1.0 op_sel_hi:[1,0]
	v_pk_mul_f32 v[4:5], v[4:5], v[168:169] op_sel_hi:[1,0]
	v_pk_mul_f32 v[2:3], v[2:3], v[168:169] op_sel_hi:[1,0]
	v_pk_fma_f32 v[32:33], v[104:105], v[32:33], v[108:109]
	v_pk_fma_f32 v[30:31], v[102:103], v[30:31], v[106:107]
	s_waitcnt vmcnt(11)
	v_pk_fma_f32 v[8:9], v[8:9], v[34:35], v[152:153]
	v_pk_fma_f32 v[6:7], v[6:7], v[36:37], v[150:151]
	s_waitcnt vmcnt(10)
	v_pk_mul_f32 v[2:3], v[2:3], v[154:155]
	v_pk_mul_f32 v[4:5], v[4:5], v[156:157]
	s_waitcnt vmcnt(9)
	v_pk_add_f32 v[34:35], v[160:161], 1.0 op_sel_hi:[1,0]
	v_pk_add_f32 v[36:37], v[158:159], 1.0 op_sel_hi:[1,0]
	s_waitcnt vmcnt(8)
	v_pk_fma_f32 v[4:5], v[4:5], v[34:35], v[164:165]
	v_pk_fma_f32 v[2:3], v[2:3], v[36:37], v[162:163]
	v_cvt_pk_bf16_f32 v30, v30, v31
	v_cvt_pk_bf16_f32 v31, v32, v33
	v_lshl_add_u64 v[32:33], v[50:51], 0, v[166:167]
	v_cvt_pk_bf16_f32 v14, v14, v15
	v_cvt_pk_bf16_f32 v15, v16, v17
	v_cvt_pk_bf16_f32 v26, v26, v27
	v_cvt_pk_bf16_f32 v27, v28, v29
	v_cvt_pk_bf16_f32 v22, v22, v23
	v_cvt_pk_bf16_f32 v23, v24, v25
	global_store_dwordx2 v[32:33], v[14:15], off offset:1536
	v_cvt_pk_bf16_f32 v14, v18, v19
	v_cvt_pk_bf16_f32 v15, v20, v21
	v_cvt_pk_bf16_f32 v10, v10, v11
	v_cvt_pk_bf16_f32 v11, v12, v13
	v_cvt_pk_bf16_f32 v6, v6, v7
	v_cvt_pk_bf16_f32 v7, v8, v9
	v_cvt_pk_bf16_f32 v2, v2, v3
	v_cvt_pk_bf16_f32 v3, v4, v5
	global_store_dwordx2 v[32:33], v[30:31], off
	global_store_dwordx2 v[32:33], v[26:27], off offset:512
	global_store_dwordx2 v[32:33], v[22:23], off offset:1024
	global_store_dwordx2 v[32:33], v[14:15], off offset:2048
	global_store_dwordx2 v[32:33], v[10:11], off offset:2560
	global_store_dwordx2 v[32:33], v[6:7], off offset:3072
	global_store_dwordx2 v[32:33], v[2:3], off offset:3584
	s_cbranch_scc1 .Ln1_top
	s_waitcnt vmcnt(0)
